# v8: + final norm g/ga hoisted, accumulator zeroing as v_mov_b64 pairs in the GEMM tile headers
# speedup vs baseline: 1.0168x; 1.0048x over previous
.LBB0_545:
	s_ashr_i32 s15, s14, 31
	s_lshl_b64 s[16:17], s[14:15], 18
	s_add_u32 s16, s30, s16
	s_addc_u32 s17, s31, s17
	s_and_b64 s[18:19], s[2:3], exec
	s_cselect_b32 s1, s17, s25
	s_cselect_b32 s15, s16, s24
	s_ashr_i32 s13, s12, 31
	s_lshl_b64 s[18:19], s[12:13], 18
	s_add_u32 s18, s34, s18
	s_addc_u32 s19, s35, s19
	s_and_b64 s[26:27], s[2:3], exec
	s_cselect_b32 s13, s19, s23
	s_cselect_b32 s33, s18, s22
	s_add_u32 s59, s22, 0x100
	s_addc_u32 s60, s23, 0
	s_add_u32 s22, s24, 0x80
	v_mov_b32_e32 v2, 0
	s_addc_u32 s23, s25, 0
	s_mov_b32 s61, -2
	v_mov_b32_e32 v3, v2
	v_mov_b64_e32 v[4:5], v[2:3]
	v_mov_b64_e32 v[6:7], v[2:3]
	v_mov_b64_e32 v[8:9], v[2:3]
	v_mov_b64_e32 v[14:15], v[2:3]
	v_mov_b64_e32 v[16:17], v[2:3]
	v_mov_b64_e32 v[22:23], v[2:3]
	v_mov_b64_e32 v[24:25], v[2:3]
	v_mov_b64_e32 v[30:31], v[2:3]
	s_waitcnt vmcnt(0)
	v_mov_b64_e32 v[32:33], v[2:3]
	v_mov_b64_e32 v[38:39], v[2:3]
	v_mov_b64_e32 v[40:41], v[2:3]
	v_mov_b64_e32 v[46:47], v[2:3]
	v_mov_b64_e32 v[48:49], v[2:3]
	v_mov_b64_e32 v[54:55], v[2:3]
	v_mov_b64_e32 v[56:57], v[2:3]
	v_mov_b64_e32 v[10:11], v[2:3]
	v_mov_b64_e32 v[12:13], v[2:3]
	v_mov_b64_e32 v[18:19], v[2:3]
	v_mov_b64_e32 v[20:21], v[2:3]
	v_mov_b64_e32 v[26:27], v[2:3]
	v_mov_b64_e32 v[28:29], v[2:3]
	v_mov_b64_e32 v[34:35], v[2:3]
	v_mov_b64_e32 v[36:37], v[2:3]
	v_mov_b64_e32 v[42:43], v[2:3]
	v_mov_b64_e32 v[44:45], v[2:3]
	v_mov_b64_e32 v[50:51], v[2:3]
	v_mov_b64_e32 v[52:53], v[2:3]
	v_mov_b64_e32 v[58:59], v[2:3]
	v_mov_b64_e32 v[60:61], v[2:3]
	v_mov_b64_e32 v[62:63], v[2:3]
	v_mov_b64_e32 v[64:65], v[2:3]
	v_mov_b64_e32 v[66:67], v[2:3]
	v_mov_b64_e32 v[68:69], v[2:3]
	v_mov_b64_e32 v[70:71], v[2:3]
	v_mov_b64_e32 v[72:73], v[2:3]
	v_mov_b64_e32 v[78:79], v[2:3]
	v_mov_b64_e32 v[80:81], v[2:3]
	v_mov_b64_e32 v[86:87], v[2:3]
	v_mov_b64_e32 v[88:89], v[2:3]
	v_mov_b64_e32 v[94:95], v[2:3]
	v_mov_b64_e32 v[96:97], v[2:3]
	v_mov_b64_e32 v[102:103], v[2:3]
	v_mov_b64_e32 v[104:105], v[2:3]
	v_mov_b64_e32 v[114:115], v[2:3]
	v_mov_b64_e32 v[116:117], v[2:3]
	v_mov_b64_e32 v[118:119], v[2:3]
	v_mov_b64_e32 v[120:121], v[2:3]
	v_mov_b64_e32 v[74:75], v[2:3]
	v_mov_b64_e32 v[76:77], v[2:3]
	v_mov_b64_e32 v[82:83], v[2:3]
	v_mov_b64_e32 v[84:85], v[2:3]
	v_mov_b64_e32 v[90:91], v[2:3]
	v_mov_b64_e32 v[92:93], v[2:3]
	v_mov_b64_e32 v[98:99], v[2:3]
	v_mov_b64_e32 v[100:101], v[2:3]
	v_mov_b64_e32 v[106:107], v[2:3]
	v_mov_b64_e32 v[108:109], v[2:3]
	v_mov_b64_e32 v[110:111], v[2:3]
	v_mov_b64_e32 v[112:113], v[2:3]
	v_mov_b64_e32 v[122:123], v[2:3]
	v_mov_b64_e32 v[124:125], v[2:3]
	v_mov_b64_e32 v[126:127], v[2:3]
	v_mov_b64_e32 v[128:129], v[2:3]

.LBB0_978:
	s_ashr_i32 s19, s18, 31
	s_lshl_b64 s[20:21], s[18:19], 19
	s_add_u32 s20, s34, s20
	s_addc_u32 s21, s35, s21
	s_and_b64 s[22:23], s[2:3], exec
	s_cselect_b32 s19, s21, s27
	s_cselect_b32 s60, s20, s26
	s_ashr_i32 s17, s16, 31
	s_lshl_b64 s[22:23], s[16:17], 19
	s_add_u32 s22, s31, s22
	s_addc_u32 s23, s33, s23
	s_and_b64 s[28:29], s[2:3], exec
	s_cselect_b32 s17, s23, s25
	s_cselect_b32 s61, s22, s24
	s_add_u32 s62, s24, 0x100
	s_addc_u32 s63, s25, 0
	s_add_u32 s24, s26, 0x80
	v_mov_b32_e32 v2, 0
	s_addc_u32 s25, s27, 0
	s_mov_b32 s64, -2
	v_mov_b32_e32 v3, v2
	v_mov_b64_e32 v[4:5], v[2:3]
	v_mov_b64_e32 v[6:7], v[2:3]
	v_mov_b64_e32 v[8:9], v[2:3]
	v_mov_b64_e32 v[14:15], v[2:3]
	v_mov_b64_e32 v[16:17], v[2:3]
	v_mov_b64_e32 v[22:23], v[2:3]
	v_mov_b64_e32 v[24:25], v[2:3]
	v_mov_b64_e32 v[34:35], v[2:3]
	v_mov_b64_e32 v[36:37], v[2:3]
	v_mov_b64_e32 v[38:39], v[2:3]
	v_mov_b64_e32 v[40:41], v[2:3]
	v_mov_b64_e32 v[50:51], v[2:3]
	v_mov_b64_e32 v[52:53], v[2:3]
	v_mov_b64_e32 v[54:55], v[2:3]
	v_mov_b64_e32 v[56:57], v[2:3]
	v_mov_b64_e32 v[10:11], v[2:3]
	v_mov_b64_e32 v[12:13], v[2:3]
	v_mov_b64_e32 v[18:19], v[2:3]
	v_mov_b64_e32 v[20:21], v[2:3]
	v_mov_b64_e32 v[26:27], v[2:3]
	v_mov_b64_e32 v[28:29], v[2:3]
	v_mov_b64_e32 v[30:31], v[2:3]
	v_mov_b64_e32 v[32:33], v[2:3]
	v_mov_b64_e32 v[42:43], v[2:3]
	v_mov_b64_e32 v[44:45], v[2:3]
	v_mov_b64_e32 v[46:47], v[2:3]
	v_mov_b64_e32 v[48:49], v[2:3]
	v_mov_b64_e32 v[58:59], v[2:3]
	v_mov_b64_e32 v[60:61], v[2:3]
	v_mov_b64_e32 v[62:63], v[2:3]
	v_mov_b64_e32 v[64:65], v[2:3]
	v_mov_b64_e32 v[82:83], v[2:3]
	v_mov_b64_e32 v[84:85], v[2:3]
	s_waitcnt vmcnt(0)
	v_mov_b64_e32 v[86:87], v[2:3]
	v_mov_b64_e32 v[88:89], v[2:3]
	v_mov_b64_e32 v[94:95], v[2:3]
	v_mov_b64_e32 v[96:97], v[2:3]
	v_mov_b64_e32 v[102:103], v[2:3]
	v_mov_b64_e32 v[104:105], v[2:3]
	v_mov_b64_e32 v[114:115], v[2:3]
	v_mov_b64_e32 v[116:117], v[2:3]
	v_mov_b64_e32 v[118:119], v[2:3]
	v_mov_b64_e32 v[120:121], v[2:3]
	v_mov_b64_e32 v[130:131], v[2:3]
	v_mov_b64_e32 v[132:133], v[2:3]
	v_mov_b64_e32 v[134:135], v[2:3]
	v_mov_b64_e32 v[136:137], v[2:3]
	v_mov_b64_e32 v[90:91], v[2:3]
	v_mov_b64_e32 v[92:93], v[2:3]
	v_mov_b64_e32 v[98:99], v[2:3]
	v_mov_b64_e32 v[100:101], v[2:3]
	v_mov_b64_e32 v[106:107], v[2:3]
	v_mov_b64_e32 v[108:109], v[2:3]
	v_mov_b64_e32 v[110:111], v[2:3]
	v_mov_b64_e32 v[112:113], v[2:3]
	v_mov_b64_e32 v[122:123], v[2:3]
	v_mov_b64_e32 v[124:125], v[2:3]
	v_mov_b64_e32 v[126:127], v[2:3]
	v_mov_b64_e32 v[128:129], v[2:3]
	v_mov_b64_e32 v[138:139], v[2:3]
	v_mov_b64_e32 v[140:141], v[2:3]
	v_mov_b64_e32 v[142:143], v[2:3]
	v_mov_b64_e32 v[144:145], v[2:3]

.LBB0_1242:
	s_ashr_i32 s23, s22, 31
	s_lshl_b64 s[24:25], s[22:23], 21
	s_add_u32 s23, s1, s24
	s_addc_u32 s30, s33, s25
	s_ashr_i32 s21, s20, 31
	s_lshl_b64 s[24:25], s[20:21], 18
	s_add_u32 s24, s23, s24
	s_addc_u32 s25, s30, s25
	s_and_b64 s[30:31], s[2:3], exec
	s_cselect_b32 s21, s25, s29
	s_cselect_b32 s23, s24, s28
	s_lshl_b32 s64, s63, 10
	s_add_u32 s65, s28, 0x100
	v_mov_b32_e32 v2, 0
	s_addc_u32 s66, s29, 0
	s_mov_b32 s67, -2
	s_mov_b64 s[28:29], s[12:13]
	v_mov_b32_e32 v3, v2
	v_mov_b64_e32 v[4:5], v[2:3]
	v_mov_b64_e32 v[10:11], v[2:3]
	v_mov_b64_e32 v[12:13], v[2:3]
	v_mov_b64_e32 v[18:19], v[2:3]
	v_mov_b64_e32 v[20:21], v[2:3]
	v_mov_b64_e32 v[26:27], v[2:3]
	v_mov_b64_e32 v[28:29], v[2:3]
	v_mov_b64_e32 v[34:35], v[2:3]
	v_mov_b64_e32 v[36:37], v[2:3]
	v_mov_b64_e32 v[42:43], v[2:3]
	v_mov_b64_e32 v[44:45], v[2:3]
	v_mov_b64_e32 v[50:51], v[2:3]
	v_mov_b64_e32 v[52:53], v[2:3]
	v_mov_b64_e32 v[58:59], v[2:3]
	v_mov_b64_e32 v[60:61], v[2:3]
	v_mov_b64_e32 v[6:7], v[2:3]
	v_mov_b64_e32 v[8:9], v[2:3]
	v_mov_b64_e32 v[14:15], v[2:3]
	v_mov_b64_e32 v[16:17], v[2:3]
	v_mov_b64_e32 v[22:23], v[2:3]
	v_mov_b64_e32 v[24:25], v[2:3]
	v_mov_b64_e32 v[30:31], v[2:3]
	v_mov_b64_e32 v[32:33], v[2:3]
	v_mov_b64_e32 v[38:39], v[2:3]
	v_mov_b64_e32 v[40:41], v[2:3]
	v_mov_b64_e32 v[46:47], v[2:3]
	v_mov_b64_e32 v[48:49], v[2:3]
	v_mov_b64_e32 v[54:55], v[2:3]
	v_mov_b64_e32 v[56:57], v[2:3]
	v_mov_b64_e32 v[62:63], v[2:3]
	v_mov_b64_e32 v[64:65], v[2:3]
	v_mov_b64_e32 v[70:71], v[2:3]
	v_mov_b64_e32 v[72:73], v[2:3]
	v_mov_b64_e32 v[86:87], v[2:3]
	v_mov_b64_e32 v[88:89], v[2:3]
	v_mov_b64_e32 v[98:99], v[2:3]
	s_waitcnt vmcnt(0)
	v_mov_b64_e32 v[100:101], v[2:3]
	v_mov_b64_e32 v[106:107], v[2:3]
	v_mov_b64_e32 v[108:109], v[2:3]
	v_mov_b64_e32 v[114:115], v[2:3]
	v_mov_b64_e32 v[116:117], v[2:3]
	v_mov_b64_e32 v[122:123], v[2:3]
	v_mov_b64_e32 v[124:125], v[2:3]
	v_mov_b64_e32 v[130:131], v[2:3]
	v_mov_b64_e32 v[132:133], v[2:3]
	v_mov_b64_e32 v[138:139], v[2:3]
	v_mov_b64_e32 v[140:141], v[2:3]
	v_mov_b64_e32 v[78:79], v[2:3]
	v_mov_b64_e32 v[80:81], v[2:3]
	v_mov_b64_e32 v[94:95], v[2:3]
	v_mov_b64_e32 v[96:97], v[2:3]
	v_mov_b64_e32 v[102:103], v[2:3]
	v_mov_b64_e32 v[104:105], v[2:3]
	v_mov_b64_e32 v[110:111], v[2:3]
	v_mov_b64_e32 v[112:113], v[2:3]
	v_mov_b64_e32 v[118:119], v[2:3]
	v_mov_b64_e32 v[120:121], v[2:3]
	v_mov_b64_e32 v[126:127], v[2:3]
	v_mov_b64_e32 v[128:129], v[2:3]
	v_mov_b64_e32 v[134:135], v[2:3]
	v_mov_b64_e32 v[136:137], v[2:3]
	v_mov_b64_e32 v[142:143], v[2:3]
	v_mov_b64_e32 v[144:145], v[2:3]

.LBB0_1348:
	s_ashr_i32 s15, s14, 31
	s_lshl_b64 s[18:19], s[14:15], 18
	s_add_u32 s18, s40, s18
	s_addc_u32 s19, s41, s19
	s_and_b64 s[20:21], s[2:3], exec
	s_cselect_b32 s15, s19, s29
	s_cselect_b32 s64, s18, s28
	s_ashr_i32 s17, s16, 31
	s_lshl_b64 s[20:21], s[16:17], 20
	s_add_u32 s17, s42, s20
	s_addc_u32 s30, s43, s21
	s_ashr_i32 s13, s12, 31
	s_lshl_b64 s[20:21], s[12:13], 18
	s_add_u32 s20, s17, s20
	s_addc_u32 s21, s30, s21
	s_and_b64 s[30:31], s[2:3], exec
	s_cselect_b32 s13, s21, s27
	s_cselect_b32 s17, s20, s26
	s_add_u32 s65, s26, 0x100
	s_addc_u32 s66, s27, 0
	s_add_u32 s26, s28, 0x80
	v_mov_b32_e32 v2, 0
	s_addc_u32 s27, s29, 0
	s_mov_b32 s67, -2
	v_mov_b32_e32 v3, v2
	v_mov_b64_e32 v[4:5], v[2:3]
	v_mov_b64_e32 v[6:7], v[2:3]
	v_mov_b64_e32 v[8:9], v[2:3]
	v_mov_b64_e32 v[10:11], v[2:3]
	v_mov_b64_e32 v[12:13], v[2:3]
	v_mov_b64_e32 v[14:15], v[2:3]
	v_mov_b64_e32 v[16:17], v[2:3]
	v_mov_b64_e32 v[18:19], v[2:3]
	v_mov_b64_e32 v[20:21], v[2:3]
	v_mov_b64_e32 v[22:23], v[2:3]
	v_mov_b64_e32 v[24:25], v[2:3]
	v_mov_b64_e32 v[26:27], v[2:3]
	v_mov_b64_e32 v[28:29], v[2:3]
	v_mov_b64_e32 v[30:31], v[2:3]
	v_mov_b64_e32 v[32:33], v[2:3]
	v_mov_b64_e32 v[58:59], v[2:3]
	v_mov_b64_e32 v[60:61], v[2:3]
	v_mov_b64_e32 v[66:67], v[2:3]
	v_mov_b64_e32 v[68:69], v[2:3]
	v_mov_b64_e32 v[74:75], v[2:3]
	v_mov_b64_e32 v[76:77], v[2:3]
	s_waitcnt vmcnt(0)
	v_mov_b64_e32 v[78:79], v[2:3]
	v_mov_b64_e32 v[80:81], v[2:3]
	v_mov_b64_e32 v[82:83], v[2:3]
	v_mov_b64_e32 v[84:85], v[2:3]
	v_mov_b64_e32 v[86:87], v[2:3]
	v_mov_b64_e32 v[88:89], v[2:3]
	v_mov_b64_e32 v[90:91], v[2:3]
	v_mov_b64_e32 v[92:93], v[2:3]
	v_mov_b64_e32 v[94:95], v[2:3]
	v_mov_b64_e32 v[96:97], v[2:3]
	v_mov_b64_e32 v[34:35], v[2:3]
	v_mov_b64_e32 v[36:37], v[2:3]
	v_mov_b64_e32 v[38:39], v[2:3]
	v_mov_b64_e32 v[40:41], v[2:3]
	v_mov_b64_e32 v[42:43], v[2:3]
	v_mov_b64_e32 v[44:45], v[2:3]
	v_mov_b64_e32 v[46:47], v[2:3]
	v_mov_b64_e32 v[48:49], v[2:3]
	v_mov_b64_e32 v[50:51], v[2:3]
	v_mov_b64_e32 v[52:53], v[2:3]
	v_mov_b64_e32 v[54:55], v[2:3]
	v_mov_b64_e32 v[56:57], v[2:3]
	v_mov_b64_e32 v[62:63], v[2:3]
	v_mov_b64_e32 v[64:65], v[2:3]
	v_mov_b64_e32 v[70:71], v[2:3]
	v_mov_b64_e32 v[72:73], v[2:3]
	v_mov_b64_e32 v[98:99], v[2:3]
	v_mov_b64_e32 v[100:101], v[2:3]
	v_mov_b64_e32 v[102:103], v[2:3]
	v_mov_b64_e32 v[104:105], v[2:3]
	v_mov_b64_e32 v[106:107], v[2:3]
	v_mov_b64_e32 v[108:109], v[2:3]
	v_mov_b64_e32 v[110:111], v[2:3]
	v_mov_b64_e32 v[112:113], v[2:3]
	v_mov_b64_e32 v[114:115], v[2:3]
	v_mov_b64_e32 v[116:117], v[2:3]
	v_mov_b64_e32 v[118:119], v[2:3]
	v_mov_b64_e32 v[120:121], v[2:3]
	v_mov_b64_e32 v[122:123], v[2:3]
	v_mov_b64_e32 v[124:125], v[2:3]
	v_mov_b64_e32 v[126:127], v[2:3]
	v_mov_b64_e32 v[128:129], v[2:3]

.LBB0_1428:
	s_mov_b32 s2, s15
	s_mov_b32 s18, 0
	s_ashr_i32 s19, s2, 13
	s_add_i32 s19, s19, 12
	s_mul_hi_i32 s21, s19, 0x6000
	s_mulk_i32 s19, 0x6000
	s_add_u32 s20, s4, s19
	s_addc_u32 s21, s5, s21
	v_lshl_add_u64 v[14:15], s[20:21], 0, v[4:5]
	v_lshl_add_u64 v[34:35], v[14:15], 0, s[0:1]
	global_load_dwordx4 v[146:149], v[34:35], off
	global_load_dwordx4 v[150:153], v[34:35], off offset:1024
	global_load_dwordx4 v[154:157], v[34:35], off offset:2048
	global_load_dwordx4 v[158:161], v[34:35], off offset:3072
	global_load_dwordx4 v[130:133], v[10:11], off
	global_load_dwordx4 v[134:137], v[10:11], off offset:1024
	global_load_dwordx4 v[138:141], v[10:11], off offset:2048
	global_load_dwordx4 v[142:145], v[10:11], off offset:3072
	s_waitcnt vmcnt(0)
.LBB0_1429:
	s_ashr_i32 s3, s2, 31
	s_ashr_i32 s19, s2, 13
	s_lshl_b64 s[20:21], s[2:3], 11
	s_add_i32 s19, s19, 12
	v_lshl_add_u64 v[14:15], v[6:7], 0, s[20:21]
	s_mul_hi_i32 s21, s19, 0x6000
	s_mulk_i32 s19, 0x6000
	s_add_u32 s20, s4, s19
	s_addc_u32 s21, s5, s21
	s_add_i32 s22, s13, s18
	s_ashr_i32 s23, s22, 31
	v_mov_b64_e32 v[0:1], v[130:131]
	v_mov_b64_e32 v[2:3], v[132:133]
	global_load_dwordx2 v[42:43], v[14:15], off
	global_load_dwordx2 v[44:45], v[14:15], off offset:512
	global_load_dwordx2 v[46:47], v[14:15], off offset:1024
	global_load_dwordx2 v[48:49], v[14:15], off offset:1536
	v_lshl_add_u64 v[14:15], s[20:21], 0, v[4:5]
	s_lshl_b64 s[20:21], s[22:23], 2
	s_add_u32 s24, s6, s20
	v_lshl_add_u64 v[34:35], v[14:15], 0, s[0:1]
	v_add_co_u32_e32 v14, vcc, s17, v14
	s_addc_u32 s25, s7, s21
	s_nop 0
	v_addc_co_u32_e32 v15, vcc, 0, v15, vcc
	v_mov_b64_e32 v[18:19], v[150:151]
	v_mov_b64_e32 v[20:21], v[152:153]
	v_mov_b64_e32 v[22:23], v[154:155]
	v_mov_b64_e32 v[24:25], v[156:157]
	v_mov_b64_e32 v[26:27], v[146:147]
	v_mov_b64_e32 v[28:29], v[148:149]
	v_mov_b64_e32 v[30:31], v[158:159]
	v_mov_b64_e32 v[32:33], v[160:161]
	s_waitcnt vmcnt(3)
	v_lshlrev_b32_e32 v56, 16, v42
	global_load_dwordx4 v[34:37], v5, s[24:25]
	s_add_u32 s24, s10, s20
	s_addc_u32 s25, s11, s21
	s_add_u32 s20, s8, s20
	s_addc_u32 s21, s9, s21
	global_load_dword v41, v5, s[24:25]
	global_load_dword v50, v5, s[20:21]
	s_add_i32 s24, s22, 1
	s_ashr_i32 s25, s24, 31
	s_lshl_b64 s[20:21], s[24:25], 2
	s_add_u32 s24, s10, s20
	s_addc_u32 s25, s11, s21
	global_load_dwordx3 v[38:40], v5, s[24:25]
	s_add_u32 s20, s8, s20
	s_addc_u32 s21, s9, s21
	s_add_i32 s22, s22, 2
	s_ashr_i32 s23, s22, 31
	global_load_dword v52, v5, s[20:21]
	s_lshl_b64 s[20:21], s[22:23], 2
	s_add_u32 s20, s8, s20
	s_addc_u32 s21, s9, s21
	global_load_dwordx2 v[54:55], v5, s[20:21]
	v_and_b32_e32 v57, 0xffff0000, v42
	v_lshlrev_b32_e32 v42, 16, v43
	v_and_b32_e32 v43, 0xffff0000, v43
	s_waitcnt vmcnt(8)
	v_lshlrev_b32_e32 v58, 16, v44
	v_and_b32_e32 v59, 0xffff0000, v44
	v_lshlrev_b32_e32 v44, 16, v45
	v_and_b32_e32 v45, 0xffff0000, v45
	s_waitcnt vmcnt(7)
	v_lshlrev_b32_e32 v60, 16, v46
	v_and_b32_e32 v61, 0xffff0000, v46
	v_lshlrev_b32_e32 v46, 16, v47
	v_and_b32_e32 v47, 0xffff0000, v47
	s_waitcnt vmcnt(6)
	v_lshlrev_b32_e32 v62, 16, v48
	v_and_b32_e32 v63, 0xffff0000, v48
	v_lshlrev_b32_e32 v48, 16, v49
	v_and_b32_e32 v49, 0xffff0000, v49
	s_lshl_b64 s[22:23], s[2:3], 12
	v_lshl_add_u64 v[14:15], v[12:13], 0, s[22:23]
	s_add_i32 s18, s18, 4
	s_add_i32 s2, s2, 1
	s_cmp_eq_u32 s18, 64
	s_waitcnt vmcnt(5)
	v_lshlrev_b32_e32 v34, 2, v34
	v_lshlrev_b32_e32 v37, 2, v37
	v_lshlrev_b32_e32 v35, 2, v35
	v_lshlrev_b32_e32 v36, 2, v36
	v_add_u32_e32 v34, s12, v34
	v_add_u32_e32 v37, s12, v37
	v_add_u32_e32 v35, s12, v35
	v_add_u32_e32 v36, s12, v36
	ds_read_b32 v34, v34
	ds_read_b32 v51, v35
	ds_read_b32 v53, v36
	ds_read_b32 v37, v37
	s_waitcnt vmcnt(4) lgkmcnt(3)
	v_add_u32_e32 v34, v34, v41
	v_ashrrev_i32_e32 v35, 31, v34
	v_lshlrev_b64 v[34:35], 10, v[34:35]
	s_waitcnt vmcnt(2) lgkmcnt(2)
	v_add_u32_e32 v36, v51, v38
	v_lshl_add_u64 v[34:35], v[8:9], 0, v[34:35]
	s_waitcnt lgkmcnt(1)
	v_add_u32_e32 v38, v53, v39
	s_waitcnt lgkmcnt(0)
	v_add_u32_e32 v40, v37, v40
	v_ashrrev_i32_e32 v37, 31, v36
	global_load_dword v51, v[34:35], off
	global_load_dword v53, v[34:35], off offset:256
	global_load_dword v67, v[34:35], off offset:512
	global_load_dword v71, v[34:35], off offset:768
	v_ashrrev_i32_e32 v39, 31, v38
	v_ashrrev_i32_e32 v41, 31, v40
	v_lshlrev_b64 v[36:37], 10, v[36:37]
	v_lshlrev_b64 v[38:39], 10, v[38:39]
	v_lshlrev_b64 v[40:41], 10, v[40:41]
	v_lshl_add_u64 v[34:35], v[8:9], 0, v[36:37]
	v_lshl_add_u64 v[36:37], v[8:9], 0, v[38:39]
	v_lshl_add_u64 v[38:39], v[8:9], 0, v[40:41]
	global_load_dword v75, v[34:35], off
	global_load_dword v79, v[34:35], off offset:256
	global_load_dword v83, v[34:35], off offset:512
	global_load_dword v87, v[34:35], off offset:768
	global_load_dword v91, v[36:37], off
	global_load_dword v95, v[36:37], off offset:256
	global_load_dword v99, v[36:37], off offset:512
	global_load_dword v103, v[36:37], off offset:768
	global_load_dword v107, v[38:39], off
	global_load_dword v111, v[38:39], off offset:256
	global_load_dword v115, v[38:39], off offset:512
	global_load_dword v119, v[38:39], off offset:768
	s_waitcnt vmcnt(15)
	v_cvt_f32_fp8_e32 v34, v51
	v_cvt_f32_fp8_sdwa v35, v51 src0_sel:BYTE_1
	v_cvt_f32_fp8_sdwa v36, v51 src0_sel:BYTE_2
	v_cvt_f32_fp8_sdwa v37, v51 src0_sel:BYTE_3
	s_waitcnt vmcnt(14)
	v_cvt_f32_fp8_e32 v38, v53
	v_cvt_f32_fp8_sdwa v39, v53 src0_sel:BYTE_1
	v_cvt_f32_fp8_sdwa v40, v53 src0_sel:BYTE_2
	v_cvt_f32_fp8_sdwa v41, v53 src0_sel:BYTE_3
	s_waitcnt vmcnt(11)
	v_cvt_f32_fp8_e32 v72, v75
	v_cvt_f32_fp8_sdwa v73, v75 src0_sel:BYTE_1
	v_cvt_f32_fp8_sdwa v74, v75 src0_sel:BYTE_2
	v_cvt_f32_fp8_sdwa v75, v75 src0_sel:BYTE_3
	s_waitcnt vmcnt(10)
	v_cvt_f32_fp8_e32 v76, v79
	v_cvt_f32_fp8_sdwa v77, v79 src0_sel:BYTE_1
	v_cvt_f32_fp8_sdwa v78, v79 src0_sel:BYTE_2
	v_cvt_f32_fp8_sdwa v79, v79 src0_sel:BYTE_3
	v_cvt_f32_fp8_e32 v64, v67
	v_cvt_f32_fp8_sdwa v65, v67 src0_sel:BYTE_1
	v_cvt_f32_fp8_sdwa v66, v67 src0_sel:BYTE_2
	v_cvt_f32_fp8_sdwa v67, v67 src0_sel:BYTE_3
	v_cvt_f32_fp8_e32 v68, v71
	v_cvt_f32_fp8_sdwa v69, v71 src0_sel:BYTE_1
	v_cvt_f32_fp8_sdwa v70, v71 src0_sel:BYTE_2
	v_cvt_f32_fp8_sdwa v71, v71 src0_sel:BYTE_3
	s_waitcnt vmcnt(7)
	v_cvt_f32_fp8_e32 v88, v91
	v_cvt_f32_fp8_sdwa v89, v91 src0_sel:BYTE_1
	v_cvt_f32_fp8_sdwa v90, v91 src0_sel:BYTE_2
	v_cvt_f32_fp8_sdwa v91, v91 src0_sel:BYTE_3
	s_waitcnt vmcnt(6)
	v_cvt_f32_fp8_e32 v92, v95
	v_cvt_f32_fp8_sdwa v93, v95 src0_sel:BYTE_1
	v_cvt_f32_fp8_sdwa v94, v95 src0_sel:BYTE_2
	v_cvt_f32_fp8_sdwa v95, v95 src0_sel:BYTE_3
	v_cvt_f32_fp8_e32 v80, v83
	v_cvt_f32_fp8_sdwa v81, v83 src0_sel:BYTE_1
	v_cvt_f32_fp8_sdwa v82, v83 src0_sel:BYTE_2
	v_cvt_f32_fp8_sdwa v83, v83 src0_sel:BYTE_3
	v_cvt_f32_fp8_e32 v84, v87
	v_cvt_f32_fp8_sdwa v85, v87 src0_sel:BYTE_1
	s_waitcnt vmcnt(3)
	v_cvt_f32_fp8_e32 v104, v107
	v_cvt_f32_fp8_sdwa v105, v107 src0_sel:BYTE_1
	v_cvt_f32_fp8_sdwa v106, v107 src0_sel:BYTE_2
	v_cvt_f32_fp8_sdwa v107, v107 src0_sel:BYTE_3
	s_waitcnt vmcnt(2)
	v_cvt_f32_fp8_e32 v108, v111
	v_cvt_f32_fp8_sdwa v109, v111 src0_sel:BYTE_1
	v_cvt_f32_fp8_sdwa v110, v111 src0_sel:BYTE_2
	v_cvt_f32_fp8_sdwa v111, v111 src0_sel:BYTE_3
	v_cvt_f32_fp8_sdwa v86, v87 src0_sel:BYTE_2
	v_cvt_f32_fp8_sdwa v87, v87 src0_sel:BYTE_3
	v_cvt_f32_fp8_e32 v96, v99
	v_cvt_f32_fp8_sdwa v97, v99 src0_sel:BYTE_1
	v_cvt_f32_fp8_sdwa v98, v99 src0_sel:BYTE_2
	v_cvt_f32_fp8_sdwa v99, v99 src0_sel:BYTE_3
	v_cvt_f32_fp8_e32 v100, v103
	v_cvt_f32_fp8_sdwa v101, v103 src0_sel:BYTE_1
	v_pk_fma_f32 v[34:35], v[50:51], v[34:35], 0 op_sel_hi:[0,1,0]
	v_pk_fma_f32 v[36:37], v[50:51], v[36:37], 0 op_sel_hi:[0,1,0]
	v_pk_fma_f32 v[38:39], v[50:51], v[38:39], 0 op_sel_hi:[0,1,0]
	v_pk_fma_f32 v[40:41], v[50:51], v[40:41], 0 op_sel_hi:[0,1,0]
	v_cvt_f32_fp8_sdwa v102, v103 src0_sel:BYTE_2
	v_cvt_f32_fp8_sdwa v103, v103 src0_sel:BYTE_3
	s_waitcnt vmcnt(1)
	v_cvt_f32_fp8_e32 v112, v115
	v_cvt_f32_fp8_sdwa v113, v115 src0_sel:BYTE_1
	v_cvt_f32_fp8_sdwa v114, v115 src0_sel:BYTE_2
	v_cvt_f32_fp8_sdwa v115, v115 src0_sel:BYTE_3
	s_waitcnt vmcnt(0)
	v_cvt_f32_fp8_e32 v116, v119
	v_cvt_f32_fp8_sdwa v117, v119 src0_sel:BYTE_1
	v_pk_fma_f32 v[36:37], v[52:53], v[74:75], v[36:37] op_sel_hi:[0,1,1]
	v_pk_fma_f32 v[34:35], v[52:53], v[72:73], v[34:35] op_sel_hi:[0,1,1]
	v_pk_fma_f32 v[40:41], v[52:53], v[78:79], v[40:41] op_sel_hi:[0,1,1]
	v_pk_fma_f32 v[38:39], v[52:53], v[76:77], v[38:39] op_sel_hi:[0,1,1]
	v_cvt_f32_fp8_sdwa v118, v119 src0_sel:BYTE_2
	v_cvt_f32_fp8_sdwa v119, v119 src0_sel:BYTE_3
	v_pk_fma_f32 v[66:67], v[50:51], v[66:67], 0 op_sel_hi:[0,1,0]
	v_pk_fma_f32 v[64:65], v[50:51], v[64:65], 0 op_sel_hi:[0,1,0]
	v_pk_fma_f32 v[70:71], v[50:51], v[70:71], 0 op_sel_hi:[0,1,0]
	v_pk_fma_f32 v[50:51], v[50:51], v[68:69], 0 op_sel_hi:[0,1,0]
	v_pk_fma_f32 v[34:35], v[54:55], v[88:89], v[34:35] op_sel_hi:[0,1,1]
	v_pk_fma_f32 v[36:37], v[54:55], v[90:91], v[36:37] op_sel_hi:[0,1,1]
	v_pk_fma_f32 v[38:39], v[54:55], v[92:93], v[38:39] op_sel_hi:[0,1,1]
	v_pk_fma_f32 v[40:41], v[54:55], v[94:95], v[40:41] op_sel_hi:[0,1,1]
	v_pk_fma_f32 v[64:65], v[52:53], v[80:81], v[64:65] op_sel_hi:[0,1,1]
	v_pk_fma_f32 v[66:67], v[52:53], v[82:83], v[66:67] op_sel_hi:[0,1,1]
	v_pk_fma_f32 v[50:51], v[52:53], v[84:85], v[50:51] op_sel_hi:[0,1,1]
	v_pk_fma_f32 v[36:37], v[54:55], v[106:107], v[36:37] op_sel:[1,0,0]
	v_pk_fma_f32 v[34:35], v[54:55], v[104:105], v[34:35] op_sel:[1,0,0]
	v_pk_fma_f32 v[40:41], v[54:55], v[110:111], v[40:41] op_sel:[1,0,0]
	v_pk_fma_f32 v[38:39], v[54:55], v[108:109], v[38:39] op_sel:[1,0,0]
	v_pk_fma_f32 v[52:53], v[52:53], v[86:87], v[70:71] op_sel_hi:[0,1,1]
	v_pk_fma_f32 v[66:67], v[54:55], v[98:99], v[66:67] op_sel_hi:[0,1,1]
	v_pk_fma_f32 v[64:65], v[54:55], v[96:97], v[64:65] op_sel_hi:[0,1,1]
	v_pk_fma_f32 v[50:51], v[54:55], v[100:101], v[50:51] op_sel_hi:[0,1,1]
	v_pk_fma_f32 v[26:27], v[34:35], v[26:27], v[56:57]
	v_pk_fma_f32 v[28:29], v[36:37], v[28:29], v[42:43]
	v_pk_fma_f32 v[18:19], v[38:39], v[18:19], v[58:59]
	v_pk_fma_f32 v[20:21], v[40:41], v[20:21], v[44:45]
	v_pk_fma_f32 v[52:53], v[54:55], v[102:103], v[52:53] op_sel_hi:[0,1,1]
	v_pk_fma_f32 v[64:65], v[54:55], v[112:113], v[64:65] op_sel:[1,0,0]
	v_pk_fma_f32 v[66:67], v[54:55], v[114:115], v[66:67] op_sel:[1,0,0]
	v_pk_fma_f32 v[50:51], v[54:55], v[116:117], v[50:51] op_sel:[1,0,0]
	v_pk_mul_f32 v[34:35], v[28:29], v[28:29]
	v_pk_mul_f32 v[36:37], v[26:27], v[26:27]
	v_pk_mul_f32 v[38:39], v[20:21], v[20:21]
	v_pk_mul_f32 v[40:41], v[18:19], v[18:19]
	v_pk_fma_f32 v[52:53], v[54:55], v[118:119], v[52:53] op_sel:[1,0,0]
	v_pk_fma_f32 v[24:25], v[66:67], v[24:25], v[46:47]
	v_pk_fma_f32 v[22:23], v[64:65], v[22:23], v[60:61]
	v_pk_fma_f32 v[30:31], v[50:51], v[30:31], v[62:63]
	v_pk_mov_b32 v[46:47], v[36:37], v[34:35] op_sel:[1,0]
	v_mov_b32_e32 v37, v35
	v_pk_mov_b32 v[34:35], v[40:41], v[38:39] op_sel:[1,0]
	v_mov_b32_e32 v41, v39
	v_pk_fma_f32 v[32:33], v[52:53], v[32:33], v[48:49]
	v_mul_f32_e32 v45, v30, v30
	v_mul_f32_e32 v42, v23, v23
	v_mul_f32_e32 v44, v25, v25
	v_pk_add_f32 v[36:37], v[46:47], v[36:37]
	v_pk_add_f32 v[34:35], v[34:35], v[40:41]
	v_mul_f32_e32 v48, v31, v31
	v_mul_f32_e32 v49, v32, v32
	v_mul_f32_e32 v50, v33, v33
	v_pk_fma_f32 v[38:39], v[22:23], v[22:23], v[42:43] op_sel_hi:[1,1,0]
	v_pk_fma_f32 v[42:43], v[24:25], v[24:25], v[44:45] op_sel_hi:[1,1,0]
	v_pk_add_f32 v[36:37], v[36:37], v[36:37] op_sel:[0,1] op_sel_hi:[1,0]
	v_pk_add_f32 v[34:35], v[34:35], v[34:35] op_sel:[0,1] op_sel_hi:[1,0]
	v_mov_b32_e32 v39, v49
	v_mov_b32_e32 v43, v50
	v_mov_b32_e32 v37, v45
	v_mov_b32_e32 v35, v48
	v_pk_add_f32 v[38:39], v[38:39], v[42:43]
	v_pk_add_f32 v[34:35], v[36:37], v[34:35]
	s_nop 0
	v_pk_add_f32 v[34:35], v[34:35], v[38:39]
	s_nop 0
	v_add_f32_e32 v34, v34, v35
	s_nop 1
	v_add_f32_dpp v34, v34, v34 quad_perm:[1,0,3,2] row_mask:0xf bank_mask:0xf bound_ctrl:1
	s_nop 1
	v_add_f32_dpp v34, v34, v34 quad_perm:[2,3,0,1] row_mask:0xf bank_mask:0xf bound_ctrl:1
	s_nop 1
	v_add_f32_dpp v34, v34, v34 row_half_mirror row_mask:0xf bank_mask:0xf bound_ctrl:1
	s_nop 1
	v_add_f32_dpp v34, v34, v34 row_mirror row_mask:0xf bank_mask:0xf bound_ctrl:1
	ds_swizzle_b32 v35, v34 offset:swizzle(SWAP,16)
	s_waitcnt lgkmcnt(0)
	v_add_f32_e32 v34, v34, v35
	ds_bpermute_b32 v35, v16, v34
	s_waitcnt lgkmcnt(0)
	v_add_f32_e32 v34, v34, v35
	v_fmamk_f32 v34, v34, 0x3a800000, v17
	v_rsq_f32_e32 v34, v34
	s_nop 0
	v_pk_mul_f32 v[26:27], v[26:27], v[34:35] op_sel_hi:[1,0]
	v_pk_mul_f32 v[28:29], v[28:29], v[34:35] op_sel_hi:[1,0]
	v_pk_mul_f32 v[0:1], v[0:1], v[26:27]
	v_pk_mul_f32 v[2:3], v[2:3], v[28:29]
	global_store_dwordx4 v[14:15], v[0:3], off
	s_nop 1
	v_mov_b64_e32 v[0:1], v[134:135]
	v_mov_b64_e32 v[2:3], v[136:137]
	v_pk_mul_f32 v[20:21], v[20:21], v[34:35] op_sel_hi:[1,0]
	v_pk_mul_f32 v[18:19], v[18:19], v[34:35] op_sel_hi:[1,0]
	s_nop 0
	v_pk_mul_f32 v[2:3], v[2:3], v[20:21]
	v_pk_mul_f32 v[0:1], v[0:1], v[18:19]
	global_store_dwordx4 v[14:15], v[0:3], off offset:1024
	s_nop 1
	v_mov_b64_e32 v[0:1], v[138:139]
	v_mov_b64_e32 v[2:3], v[140:141]
	v_pk_mul_f32 v[18:19], v[24:25], v[34:35] op_sel_hi:[1,0]
	v_pk_mul_f32 v[20:21], v[22:23], v[34:35] op_sel_hi:[1,0]
	s_nop 0
	v_pk_mul_f32 v[2:3], v[2:3], v[18:19]
	v_pk_mul_f32 v[0:1], v[0:1], v[20:21]
	global_store_dwordx4 v[14:15], v[0:3], off offset:2048
	s_nop 1
	v_mov_b64_e32 v[0:1], v[142:143]
	v_mov_b64_e32 v[2:3], v[144:145]
	v_pk_mul_f32 v[18:19], v[32:33], v[34:35] op_sel_hi:[1,0]
	v_pk_mul_f32 v[20:21], v[30:31], v[34:35] op_sel_hi:[1,0]
	s_nop 0
	v_pk_mul_f32 v[2:3], v[2:3], v[18:19]
	v_pk_mul_f32 v[0:1], v[0:1], v[20:21]
	global_store_dwordx4 v[14:15], v[0:3], off offset:3072
	s_cbranch_scc0 .LBB0_1429
	s_add_i32 s88, s88, s91
	s_add_i32 s13, s13, s14
	s_add_i32 s15, s15, s16
	s_cmpk_gt_i32 s88, 0xff
	s_cbranch_scc0 .LBB0_1428
